# NA bias lookups batched (16 masked LDS reads in flight, one wait) + MLA attention inner loops: 8 K fragments / 5 V fragments prefetched from LDS with counted lgkmcnt waits
# baseline (speedup 1.0000x reference)
.LBB0_720:
	s_andn2_b64 vcc, exec, s[48:49]
	s_cbranch_vccnz .LBB0_754
	s_sub_i32 s46, s87, s62
	s_mulk_i32 s46, 0x7c
	s_add_i32 s46, s46, 0
	s_add_i32 s46, s46, 0x11800
	v_mov_b32_e32 v5, 0xf149f2ca
	v_lshl_add_u32 v4, v200, 2, s46
	v_mov_b32_e32 v6, 0xf149f2ca
	v_mov_b32_e32 v7, 0xf149f2ca
	v_mov_b32_e32 v8, 0xf149f2ca
	v_mov_b32_e32 v9, 0xf149f2ca
	v_mov_b32_e32 v10, 0xf149f2ca
	v_mov_b32_e32 v11, 0xf149f2ca
	v_mov_b32_e32 v12, 0xf149f2ca
	v_mov_b32_e32 v13, 0xf149f2ca
	v_mov_b32_e32 v14, 0xf149f2ca
	v_mov_b32_e32 v15, 0xf149f2ca
	v_mov_b32_e32 v16, 0xf149f2ca
	v_mov_b32_e32 v17, 0xf149f2ca
	v_mov_b32_e32 v96, 0xf149f2ca
	v_mov_b32_e32 v99, 0xf149f2ca
	v_mov_b32_e32 v98, 0xf149f2ca
	s_mov_b64 s[46:47], exec
	s_and_b64 exec, s[46:47], s[12:13]
	ds_read_b32 v6, v4 offset:928
	s_and_b64 exec, s[46:47], s[14:15]
	ds_read_b32 v5, v4 offset:932
	s_and_b64 exec, s[46:47], s[16:17]
	ds_read_b32 v8, v4 offset:936
	s_and_b64 exec, s[46:47], s[18:19]
	ds_read_b32 v7, v4 offset:940
	s_and_b64 exec, s[46:47], s[20:21]
	ds_read_b32 v10, v4 offset:960
	s_and_b64 exec, s[46:47], s[22:23]
	ds_read_b32 v9, v4 offset:964
	s_and_b64 exec, s[46:47], s[92:93]
	ds_read_b32 v12, v4 offset:968
	s_and_b64 exec, s[46:47], s[94:95]
	ds_read_b32 v11, v4 offset:972
	s_and_b64 exec, s[46:47], s[96:97]
	ds_read_b32 v14, v4 offset:992
	s_and_b64 exec, s[46:47], s[34:35]
	ds_read_b32 v13, v4 offset:996
	s_and_b64 exec, s[46:47], s[30:31]
	ds_read_b32 v16, v4 offset:1000
	s_and_b64 exec, s[46:47], s[28:29]
	ds_read_b32 v15, v4 offset:1004
	s_and_b64 exec, s[46:47], s[24:25]
	ds_read_b32 v96, v4 offset:1024
	s_and_b64 exec, s[46:47], s[36:37]
	ds_read_b32 v17, v4 offset:1028
	s_and_b64 exec, s[46:47], s[38:39]
	ds_read_b32 v98, v4 offset:1032
	s_and_b64 exec, s[46:47], s[40:41]
	ds_read_b32 v99, v4 offset:1036
	s_waitcnt lgkmcnt(0)
	s_and_b64 exec, s[46:47], s[12:13]
	v_fmac_f32_e32 v6, 0x3e0293ee, v100
	s_and_b64 exec, s[46:47], s[14:15]
	v_fmac_f32_e32 v5, 0x3e0293ee, v101
	s_and_b64 exec, s[46:47], s[16:17]
	v_fmac_f32_e32 v8, 0x3e0293ee, v102
	s_and_b64 exec, s[46:47], s[18:19]
	v_fmac_f32_e32 v7, 0x3e0293ee, v103
	s_and_b64 exec, s[46:47], s[20:21]
	v_fmac_f32_e32 v10, 0x3e0293ee, v104
	s_and_b64 exec, s[46:47], s[22:23]
	v_fmac_f32_e32 v9, 0x3e0293ee, v105
	s_and_b64 exec, s[46:47], s[92:93]
	v_fmac_f32_e32 v12, 0x3e0293ee, v106
	s_and_b64 exec, s[46:47], s[94:95]
	v_fmac_f32_e32 v11, 0x3e0293ee, v107
	s_and_b64 exec, s[46:47], s[96:97]
	v_fmac_f32_e32 v14, 0x3e0293ee, v108
	s_and_b64 exec, s[46:47], s[34:35]
	v_fmac_f32_e32 v13, 0x3e0293ee, v109
	s_and_b64 exec, s[46:47], s[30:31]
	v_fmac_f32_e32 v16, 0x3e0293ee, v110
	s_and_b64 exec, s[46:47], s[28:29]
	v_fmac_f32_e32 v15, 0x3e0293ee, v111
	s_and_b64 exec, s[46:47], s[24:25]
	v_fmac_f32_e32 v96, 0x3e0293ee, v112
	s_and_b64 exec, s[46:47], s[36:37]
	v_fmac_f32_e32 v17, 0x3e0293ee, v113
	s_and_b64 exec, s[46:47], s[38:39]
	v_fmac_f32_e32 v98, 0x3e0293ee, v114
	s_and_b64 exec, s[46:47], s[40:41]
	v_fmac_f32_e32 v99, 0x3e0293ee, v115
	s_mov_b64 exec, s[46:47]
	v_max3_f32 v4, v6, s58, v5
	v_max3_f32 v4, v4, v8, v7
	v_max3_f32 v4, v4, v10, v9
	v_max3_f32 v4, v4, v12, v11
	v_max3_f32 v4, v4, v14, v13
	v_max3_f32 v4, v4, v16, v15
	v_max3_f32 v4, v4, v96, v17
	v_max3_f32 v4, v4, v98, v99
	v_mov_b32_e32 v84, v4
	s_nop 1
	v_permlane32_swap_b32_e32 v4, v84
	v_max_f32_e32 v4, v4, v4
	v_max_f32_e32 v4, v2, v4
	v_sub_f32_e32 v2, v6, v4
	v_exp_f32_e32 v84, v2
	v_sub_f32_e32 v2, v5, v4
	v_exp_f32_e32 v85, v2
	v_sub_f32_e32 v2, v8, v4
	v_exp_f32_e32 v86, v2
	v_sub_f32_e32 v5, v7, v4
	v_exp_f32_e32 v87, v5
	v_sub_f32_e32 v5, v10, v4
	v_add_f32_e32 v2, 0, v84
	v_exp_f32_e32 v88, v5
	v_sub_f32_e32 v5, v9, v4
	v_add_f32_e32 v2, v85, v2
	v_exp_f32_e32 v89, v5
	v_sub_f32_e32 v5, v12, v4
	v_add_f32_e32 v2, v86, v2
	v_exp_f32_e32 v90, v5
	v_sub_f32_e32 v5, v11, v4
	v_add_f32_e32 v2, v87, v2
	v_exp_f32_e32 v91, v5
	v_sub_f32_e32 v5, v14, v4
	v_add_f32_e32 v2, v88, v2
	v_exp_f32_e32 v92, v5
	v_sub_f32_e32 v5, v13, v4
	v_add_f32_e32 v2, v89, v2
	v_exp_f32_e32 v93, v5
	v_sub_f32_e32 v5, v16, v4
	v_add_f32_e32 v2, v90, v2
	v_exp_f32_e32 v94, v5
	v_sub_f32_e32 v5, v15, v4
	v_add_f32_e32 v2, v91, v2
	v_exp_f32_e32 v95, v5
	v_sub_f32_e32 v5, v96, v4
	v_add_f32_e32 v2, v92, v2
	v_exp_f32_e32 v96, v5
	v_sub_f32_e32 v5, v17, v4
	v_add_f32_e32 v2, v93, v2
	v_exp_f32_e32 v97, v5
	v_sub_f32_e32 v5, v98, v4
	v_add_f32_e32 v2, v94, v2
	v_exp_f32_e32 v98, v5
	v_add_f32_e32 v2, v95, v2
	v_add_f32_e32 v2, v96, v2
	v_add_f32_e32 v2, v97, v2
	v_add_f32_e32 v6, v98, v2
	v_sub_f32_e32 v5, v99, v4

.LBB0_1038:
	s_bitcmp1_b32 s22, 0
	s_cselect_b32 s23, 0xac00, 0
	s_add_i32 s23, s23, 0
	v_add3_u32 v2, s23, v228, v154
	ds_read_b128 v[4:7], v2
	ds_read_b128 v[8:11], v2 offset:32
	ds_read_b128 v[12:15], v2 offset:64
	ds_read_b128 v[238:241], v2 offset:96
	ds_read_b128 v[146:149], v2 offset:128
	ds_read_b128 v[150:153], v2 offset:160
	ds_read_b128 v[248:251], v2 offset:192
	ds_read_b128 v[252:255], v2 offset:224
	s_waitcnt lgkmcnt(7)
	v_mfma_f32_32x32x16_bf16 v[82:97], v[4:7], v[142:145], 0
	ds_read_b128 v[4:7], v2 offset:256
	s_waitcnt lgkmcnt(7)
	v_mfma_f32_32x32x16_bf16 v[82:97], v[8:11], v[138:141], v[82:97]
	ds_read_b128 v[8:11], v2 offset:288
	s_waitcnt lgkmcnt(7)
	v_mfma_f32_32x32x16_bf16 v[82:97], v[12:15], v[134:137], v[82:97]
	ds_read_b128 v[12:15], v2 offset:320
	s_waitcnt lgkmcnt(7)
	v_mfma_f32_32x32x16_bf16 v[82:97], v[238:241], v[130:133], v[82:97]
	ds_read_b128 v[238:241], v2 offset:352
	s_waitcnt lgkmcnt(7)
	v_mfma_f32_32x32x16_bf16 v[82:97], v[146:149], v[126:129], v[82:97]
	s_waitcnt lgkmcnt(6)
	v_mfma_f32_32x32x16_bf16 v[82:97], v[150:153], v[122:125], v[82:97]
	s_waitcnt lgkmcnt(5)
	v_mfma_f32_32x32x16_bf16 v[82:97], v[248:251], v[118:121], v[82:97]
	s_waitcnt lgkmcnt(4)
	v_mfma_f32_32x32x16_bf16 v[82:97], v[252:255], v[114:117], v[82:97]
	s_waitcnt lgkmcnt(3)
	v_mfma_f32_32x32x16_bf16 v[82:97], v[4:7], v[110:113], v[82:97]
	s_waitcnt lgkmcnt(2)
	v_mfma_f32_32x32x16_bf16 v[82:97], v[8:11], v[106:109], v[82:97]
	v_mov_b32_e32 v2, v236
	s_waitcnt lgkmcnt(1)
	v_mfma_f32_32x32x16_bf16 v[82:97], v[12:15], v[102:105], v[82:97]
	v_lshl_add_u64 v[12:13], s[26:27], 0, v[214:215]
	v_lshl_add_u64 v[16:17], s[26:27], 0, v[210:211]
	v_lshl_add_u64 v[242:243], s[26:27], 0, v[212:213]
	v_lshl_add_u64 v[8:9], s[26:27], 0, v[208:209]
	v_lshl_add_u64 v[10:11], s[26:27], 0, v[216:217]
	s_nop 0
	global_load_dwordx4 v[150:153], v[8:9], off
	global_load_dwordx4 v[146:149], v[10:11], off
	s_nop 0
	global_load_dwordx4 v[12:15], v[12:13], off
	s_nop 0
	global_load_dwordx4 v[8:11], v[16:17], off
	global_load_dwordx4 v[4:7], v[242:243], off
	v_max_f32_e32 v16, v2, v2
	s_waitcnt lgkmcnt(0)
	v_mfma_f32_32x32x16_bf16 v[82:97], v[238:241], v[98:101], v[82:97]
	s_nop 11
	v_max3_f32 v17, v82, s19, v83
	v_max3_f32 v17, v17, v84, v85
	v_max3_f32 v17, v17, v86, v87
	v_max3_f32 v17, v17, v88, v89
	v_max3_f32 v17, v17, v90, v91
	v_max3_f32 v17, v17, v92, v93
	v_max3_f32 v17, v17, v94, v95
	v_max3_f32 v17, v17, v96, v97
	v_mov_b32_e32 v236, v17
	s_nop 1
	v_permlane32_swap_b32_e32 v17, v236
	v_mul_f32_e32 v17, 0x3dd53b95, v17
	v_max_f32_e32 v236, v16, v17
	v_fma_f32 v16, v82, s20, -v236
	v_fma_f32 v17, v83, s20, -v236
	v_fma_f32 v241, v94, s20, -v236
	v_exp_f32_e32 v94, v16
	v_fma_f32 v82, v84, s20, -v236
	v_fma_f32 v243, v96, s20, -v236
	v_exp_f32_e32 v96, v17
	v_fma_f32 v83, v85, s20, -v236
	v_fma_f32 v239, v92, s20, -v236
	v_exp_f32_e32 v92, v82
	v_fma_f32 v84, v86, s20, -v236
	v_fma_f32 v242, v95, s20, -v236
	v_exp_f32_e32 v95, v83
	v_fma_f32 v85, v87, s20, -v236
	v_fma_f32 v86, v88, s20, -v236
	v_fma_f32 v88, v90, s20, -v236
	v_exp_f32_e32 v90, v84
	v_add_f32_e32 v16, 0, v94
	v_fma_f32 v240, v93, s20, -v236
	v_exp_f32_e32 v93, v85
	v_add_f32_e32 v16, v96, v16
	v_fma_f32 v87, v89, s20, -v236
	v_exp_f32_e32 v89, v86
	v_add_f32_e32 v16, v92, v16
	v_fma_f32 v238, v91, s20, -v236
	v_exp_f32_e32 v91, v87
	v_add_f32_e32 v16, v95, v16
	v_exp_f32_e32 v84, v88
	v_add_f32_e32 v16, v90, v16
	v_exp_f32_e32 v87, v238
	v_add_f32_e32 v16, v93, v16
	v_exp_f32_e32 v82, v239
	v_add_f32_e32 v16, v89, v16
	v_exp_f32_e32 v85, v240
	v_add_f32_e32 v16, v91, v16
	v_exp_f32_e32 v17, v241
	v_add_f32_e32 v16, v84, v16
	v_exp_f32_e32 v83, v242
	v_add_f32_e32 v16, v87, v16
	v_fma_f32 v97, v97, s20, -v236
	v_exp_f32_e32 v86, v243
	v_add_f32_e32 v16, v82, v16
	v_exp_f32_e32 v88, v97
	v_add_f32_e32 v16, v85, v16
	v_sub_f32_e32 v2, v2, v236
	v_add_f32_e32 v16, v17, v16
	v_exp_f32_e32 v2, v2
	v_add_f32_e32 v16, v83, v16
	v_add_f32_e32 v16, v86, v16
	v_add_f32_e32 v16, v88, v16
	v_mov_b32_e32 v97, v16
	v_cmp_neq_f32_e32 vcc, 1.0, v2
	s_nop 0
	v_permlane32_swap_b32_e32 v16, v97
	s_cbranch_vccz .LBB0_1040
	v_pk_mul_f32 v[80:81], v[80:81], v[2:3] op_sel_hi:[1,0]
	v_pk_mul_f32 v[78:79], v[78:79], v[2:3] op_sel_hi:[1,0]
	v_pk_mul_f32 v[76:77], v[76:77], v[2:3] op_sel_hi:[1,0]
	v_pk_mul_f32 v[74:75], v[74:75], v[2:3] op_sel_hi:[1,0]
	v_pk_mul_f32 v[72:73], v[72:73], v[2:3] op_sel_hi:[1,0]
	v_pk_mul_f32 v[70:71], v[70:71], v[2:3] op_sel_hi:[1,0]
	v_pk_mul_f32 v[68:69], v[68:69], v[2:3] op_sel_hi:[1,0]
	v_pk_mul_f32 v[66:67], v[66:67], v[2:3] op_sel_hi:[1,0]
	v_pk_mul_f32 v[64:65], v[64:65], v[2:3] op_sel_hi:[1,0]
	v_pk_mul_f32 v[62:63], v[62:63], v[2:3] op_sel_hi:[1,0]
	v_pk_mul_f32 v[60:61], v[60:61], v[2:3] op_sel_hi:[1,0]
	v_pk_mul_f32 v[58:59], v[58:59], v[2:3] op_sel_hi:[1,0]
	v_pk_mul_f32 v[56:57], v[56:57], v[2:3] op_sel_hi:[1,0]
	v_pk_mul_f32 v[54:55], v[54:55], v[2:3] op_sel_hi:[1,0]
	v_pk_mul_f32 v[52:53], v[52:53], v[2:3] op_sel_hi:[1,0]
	v_pk_mul_f32 v[50:51], v[50:51], v[2:3] op_sel_hi:[1,0]
	v_pk_mul_f32 v[48:49], v[48:49], v[2:3] op_sel_hi:[1,0]
	v_pk_mul_f32 v[46:47], v[46:47], v[2:3] op_sel_hi:[1,0]
	v_pk_mul_f32 v[44:45], v[44:45], v[2:3] op_sel_hi:[1,0]
	v_pk_mul_f32 v[42:43], v[42:43], v[2:3] op_sel_hi:[1,0]
	v_pk_mul_f32 v[40:41], v[40:41], v[2:3] op_sel_hi:[1,0]
	v_pk_mul_f32 v[38:39], v[38:39], v[2:3] op_sel_hi:[1,0]
	v_pk_mul_f32 v[36:37], v[36:37], v[2:3] op_sel_hi:[1,0]
	v_pk_mul_f32 v[34:35], v[34:35], v[2:3] op_sel_hi:[1,0]
	v_pk_mul_f32 v[32:33], v[32:33], v[2:3] op_sel_hi:[1,0]
	v_pk_mul_f32 v[30:31], v[30:31], v[2:3] op_sel_hi:[1,0]
	v_pk_mul_f32 v[28:29], v[28:29], v[2:3] op_sel_hi:[1,0]
	v_pk_mul_f32 v[26:27], v[26:27], v[2:3] op_sel_hi:[1,0]
	v_pk_mul_f32 v[24:25], v[24:25], v[2:3] op_sel_hi:[1,0]
	v_pk_mul_f32 v[22:23], v[22:23], v[2:3] op_sel_hi:[1,0]
	v_pk_mul_f32 v[20:21], v[20:21], v[2:3] op_sel_hi:[1,0]
	v_pk_mul_f32 v[18:19], v[18:19], v[2:3] op_sel_hi:[1,0]
.LBB0_1040:
	s_add_i32 s23, s18, s23
	v_add_f32_e32 v16, v16, v16
	v_fmac_f32_e32 v16, v237, v2
	v_add3_u32 v2, s23, v229, v179
	v_add_u32_e32 v239, 0x6000, v2
	v_add_u32_e32 v237, 0x7000, v2
	v_add_u32_e32 v238, 0x8800, v2
	v_add_u32_e32 v2, 0x9800, v2
	ds_read2_b64 v[240:243], v239 offset0:128 offset1:130
	ds_read2_b64 v[248:251], v237 offset0:192 offset1:194
	ds_read2_b64 v[252:255], v238 offset1:2
	v_cvt_pk_bf16_f32 v94, v94, v96
	v_cvt_pk_bf16_f32 v95, v92, v95
	v_cvt_pk_bf16_f32 v96, v90, v93
	v_cvt_pk_bf16_f32 v97, v89, v91
	v_cvt_pk_bf16_f32 v90, v84, v87
	v_cvt_pk_bf16_f32 v91, v82, v85
	v_cvt_pk_bf16_f32 v92, v17, v83
	v_cvt_pk_bf16_f32 v93, v86, v88
	ds_read2_b64 v[82:85], v2 offset0:64 offset1:66
	ds_read2_b64 v[86:89], v239 offset0:132 offset1:134
	s_add_i32 s22, s22, 1
	s_bitcmp1_b32 s22, 0
	s_cselect_b32 s23, 0xac00, 0
	s_add_i32 s23, s23, 0
	s_waitcnt lgkmcnt(4)
	v_mfma_f32_32x32x16_bf16 v[66:81], v[240:243], v[94:97], v[66:81]
	ds_read2_b64 v[240:243], v237 offset0:196 offset1:198
	v_lshl_add_u64 v[208:209], v[208:209], 0, s[10:11]
	s_waitcnt lgkmcnt(4)
	v_mfma_f32_32x32x16_bf16 v[50:65], v[248:251], v[94:97], v[50:65]
	ds_read2_b64 v[248:251], v238 offset0:4 offset1:6
	v_lshl_add_u64 v[210:211], v[210:211], 0, s[12:13]
	v_lshl_add_u64 v[212:213], v[212:213], 0, s[12:13]
	s_waitcnt lgkmcnt(4)
	v_mfma_f32_32x32x16_bf16 v[34:49], v[252:255], v[94:97], v[34:49]
	ds_read2_b64 v[252:255], v2 offset0:68 offset1:70
	v_lshl_add_u64 v[214:215], v[214:215], 0, s[10:11]
	v_lshl_add_u64 v[216:217], v[216:217], 0, s[10:11]
	s_cmp_eq_u32 s22, 35
	s_waitcnt lgkmcnt(4)
	v_mfma_f32_32x32x16_bf16 v[18:33], v[82:85], v[94:97], v[18:33]
	s_waitcnt lgkmcnt(3)
	v_mfma_f32_32x32x16_bf16 v[66:81], v[86:89], v[90:93], v[66:81]
	s_waitcnt lgkmcnt(2)
	v_mfma_f32_32x32x16_bf16 v[50:65], v[240:243], v[90:93], v[50:65]
	s_waitcnt lgkmcnt(1)
	v_mfma_f32_32x32x16_bf16 v[34:49], v[248:251], v[90:93], v[34:49]
	s_waitcnt lgkmcnt(0)
	v_mfma_f32_32x32x16_bf16 v[18:33], v[252:255], v[90:93], v[18:33]
	v_add3_u32 v2, s23, v176, v181
	s_waitcnt vmcnt(4)
	ds_write_b128 v2, v[150:153]
	v_add3_u32 v2, s23, v222, v223
	s_waitcnt vmcnt(3)
	ds_write_b128 v2, v[146:149]
	v_add3_u32 v2, s23, v224, v225
	s_waitcnt vmcnt(2)
	ds_write_b128 v2, v[12:15]
	v_add_u32_e32 v2, s23, v226
	s_waitcnt vmcnt(1)
	ds_write_b128 v2, v[8:11] offset:25600
	v_add_u32_e32 v2, s23, v227
	s_waitcnt vmcnt(0)
	ds_write_b128 v2, v[4:7] offset:25600
	s_waitcnt lgkmcnt(0)
	s_barrier
	s_cbranch_scc1 .LBB0_1042
	v_mov_b32_e32 v237, v16
	s_branch .LBB0_1038

.LBB0_2903:
	s_andn2_b64 vcc, exec, s[54:55]
	s_cbranch_vccnz .LBB0_2937
	s_sub_i32 s50, s87, s67
	s_mulk_i32 s50, 0x7c
	s_add_i32 s50, s50, 0
	s_add_i32 s50, s50, 0x11800
	v_mov_b32_e32 v5, 0xf149f2ca
	v_lshl_add_u32 v4, v199, 2, s50
	v_mov_b32_e32 v6, 0xf149f2ca
	v_mov_b32_e32 v7, 0xf149f2ca
	v_mov_b32_e32 v8, 0xf149f2ca
	v_mov_b32_e32 v9, 0xf149f2ca
	v_mov_b32_e32 v10, 0xf149f2ca
	v_mov_b32_e32 v11, 0xf149f2ca
	v_mov_b32_e32 v12, 0xf149f2ca
	v_mov_b32_e32 v13, 0xf149f2ca
	v_mov_b32_e32 v14, 0xf149f2ca
	v_mov_b32_e32 v15, 0xf149f2ca
	v_mov_b32_e32 v16, 0xf149f2ca
	v_mov_b32_e32 v17, 0xf149f2ca
	v_mov_b32_e32 v96, 0xf149f2ca
	v_mov_b32_e32 v99, 0xf149f2ca
	v_mov_b32_e32 v98, 0xf149f2ca
	s_mov_b64 s[50:51], exec
	s_and_b64 exec, s[50:51], s[6:7]
	ds_read_b32 v6, v4 offset:928
	s_and_b64 exec, s[50:51], s[8:9]
	ds_read_b32 v5, v4 offset:932
	s_and_b64 exec, s[50:51], s[10:11]
	ds_read_b32 v8, v4 offset:936
	s_and_b64 exec, s[50:51], s[12:13]
	ds_read_b32 v7, v4 offset:940
	s_and_b64 exec, s[50:51], s[14:15]
	ds_read_b32 v10, v4 offset:960
	s_and_b64 exec, s[50:51], s[16:17]
	ds_read_b32 v9, v4 offset:964
	s_and_b64 exec, s[50:51], s[18:19]
	ds_read_b32 v12, v4 offset:968
	s_and_b64 exec, s[50:51], s[20:21]
	ds_read_b32 v11, v4 offset:972
	s_and_b64 exec, s[50:51], s[22:23]
	ds_read_b32 v14, v4 offset:992
	s_and_b64 exec, s[50:51], s[36:37]
	ds_read_b32 v13, v4 offset:996
	s_and_b64 exec, s[50:51], s[38:39]
	ds_read_b32 v16, v4 offset:1000
	s_and_b64 exec, s[50:51], s[34:35]
	ds_read_b32 v15, v4 offset:1004
	s_and_b64 exec, s[50:51], s[30:31]
	ds_read_b32 v96, v4 offset:1024
	s_and_b64 exec, s[50:51], s[28:29]
	ds_read_b32 v17, v4 offset:1028
	s_and_b64 exec, s[50:51], s[24:25]
	ds_read_b32 v98, v4 offset:1032
	s_and_b64 exec, s[50:51], s[40:41]
	ds_read_b32 v99, v4 offset:1036
	s_waitcnt lgkmcnt(0)
	s_and_b64 exec, s[50:51], s[6:7]
	v_fmac_f32_e32 v6, 0x3e0293ee, v100
	s_and_b64 exec, s[50:51], s[8:9]
	v_fmac_f32_e32 v5, 0x3e0293ee, v101
	s_and_b64 exec, s[50:51], s[10:11]
	v_fmac_f32_e32 v8, 0x3e0293ee, v102
	s_and_b64 exec, s[50:51], s[12:13]
	v_fmac_f32_e32 v7, 0x3e0293ee, v103
	s_and_b64 exec, s[50:51], s[14:15]
	v_fmac_f32_e32 v10, 0x3e0293ee, v104
	s_and_b64 exec, s[50:51], s[16:17]
	v_fmac_f32_e32 v9, 0x3e0293ee, v105
	s_and_b64 exec, s[50:51], s[18:19]
	v_fmac_f32_e32 v12, 0x3e0293ee, v106
	s_and_b64 exec, s[50:51], s[20:21]
	v_fmac_f32_e32 v11, 0x3e0293ee, v107
	s_and_b64 exec, s[50:51], s[22:23]
	v_fmac_f32_e32 v14, 0x3e0293ee, v108
	s_and_b64 exec, s[50:51], s[36:37]
	v_fmac_f32_e32 v13, 0x3e0293ee, v109
	s_and_b64 exec, s[50:51], s[38:39]
	v_fmac_f32_e32 v16, 0x3e0293ee, v110
	s_and_b64 exec, s[50:51], s[34:35]
	v_fmac_f32_e32 v15, 0x3e0293ee, v111
	s_and_b64 exec, s[50:51], s[30:31]
	v_fmac_f32_e32 v96, 0x3e0293ee, v112
	s_and_b64 exec, s[50:51], s[28:29]
	v_fmac_f32_e32 v17, 0x3e0293ee, v113
	s_and_b64 exec, s[50:51], s[24:25]
	v_fmac_f32_e32 v98, 0x3e0293ee, v114
	s_and_b64 exec, s[50:51], s[40:41]
	v_fmac_f32_e32 v99, 0x3e0293ee, v115
	s_mov_b64 exec, s[50:51]
	v_max3_f32 v4, v6, s62, v5
	v_max3_f32 v4, v4, v8, v7
	v_max3_f32 v4, v4, v10, v9
	v_max3_f32 v4, v4, v12, v11
	v_max3_f32 v4, v4, v14, v13
	v_max3_f32 v4, v4, v16, v15
	v_max3_f32 v4, v4, v96, v17
	v_max3_f32 v4, v4, v98, v99
	v_mov_b32_e32 v84, v4
	s_nop 1
	v_permlane32_swap_b32_e32 v4, v84
	v_max_f32_e32 v4, v4, v4
	v_max_f32_e32 v4, v2, v4
	v_sub_f32_e32 v2, v6, v4
	v_exp_f32_e32 v84, v2
	v_sub_f32_e32 v2, v5, v4
	v_exp_f32_e32 v85, v2
	v_sub_f32_e32 v2, v8, v4
	v_exp_f32_e32 v86, v2
	v_sub_f32_e32 v5, v7, v4
	v_exp_f32_e32 v87, v5
	v_sub_f32_e32 v5, v10, v4
	v_add_f32_e32 v2, 0, v84
	v_exp_f32_e32 v88, v5
	v_sub_f32_e32 v5, v9, v4
	v_add_f32_e32 v2, v85, v2
	v_exp_f32_e32 v89, v5
	v_sub_f32_e32 v5, v12, v4
	v_add_f32_e32 v2, v86, v2
	v_exp_f32_e32 v90, v5
	v_sub_f32_e32 v5, v11, v4
	v_add_f32_e32 v2, v87, v2
	v_exp_f32_e32 v91, v5
	v_sub_f32_e32 v5, v14, v4
	v_add_f32_e32 v2, v88, v2
	v_exp_f32_e32 v92, v5
	v_sub_f32_e32 v5, v13, v4
	v_add_f32_e32 v2, v89, v2
	v_exp_f32_e32 v93, v5
	v_sub_f32_e32 v5, v16, v4
	v_add_f32_e32 v2, v90, v2
	v_exp_f32_e32 v94, v5
	v_sub_f32_e32 v5, v15, v4
	v_add_f32_e32 v2, v91, v2
	v_exp_f32_e32 v95, v5
	v_sub_f32_e32 v5, v96, v4
	v_add_f32_e32 v2, v92, v2
	v_exp_f32_e32 v96, v5
	v_sub_f32_e32 v5, v17, v4
	v_add_f32_e32 v2, v93, v2
	v_exp_f32_e32 v97, v5
	v_sub_f32_e32 v5, v98, v4
	v_add_f32_e32 v2, v94, v2
	v_exp_f32_e32 v98, v5
	v_add_f32_e32 v2, v95, v2
	v_add_f32_e32 v2, v96, v2
	v_add_f32_e32 v2, v97, v2
	v_add_f32_e32 v6, v98, v2
	v_sub_f32_e32 v5, v99, v4

.LBB0_3206:
	s_bitcmp1_b32 s23, 0
	s_cselect_b32 s24, 0xac00, 0
	s_add_i32 s24, s24, 0
	v_add3_u32 v140, s24, v209, v152
	ds_read_b128 v[222:225], v140
	ds_read_b128 v[226:229], v140 offset:32
	ds_read_b128 v[248:251], v140 offset:64
	ds_read_b128 v[252:255], v140 offset:96
	ds_read_b128 v[130:133], v140 offset:128
	ds_read_b128 v[134:137], v140 offset:160
	ds_read_b128 v[142:145], v140 offset:192
	ds_read_b128 v[146:149], v140 offset:224
	v_mov_b32_e32 v189, v187
	v_max_f32_e32 v187, v189, v189
	s_waitcnt vmcnt(0) lgkmcnt(7)
	v_mfma_f32_32x32x16_bf16 v[66:81], v[222:225], v[126:129], 0
	ds_read_b128 v[222:225], v140 offset:256
	s_waitcnt lgkmcnt(7)
	v_mfma_f32_32x32x16_bf16 v[66:81], v[226:229], v[106:109], v[66:81]
	ds_read_b128 v[226:229], v140 offset:288
	s_waitcnt lgkmcnt(7)
	v_mfma_f32_32x32x16_bf16 v[66:81], v[248:251], v[102:105], v[66:81]
	ds_read_b128 v[248:251], v140 offset:320
	s_waitcnt lgkmcnt(7)
	v_mfma_f32_32x32x16_bf16 v[66:81], v[252:255], v[98:101], v[66:81]
	ds_read_b128 v[252:255], v140 offset:352
	s_waitcnt lgkmcnt(7)
	v_mfma_f32_32x32x16_bf16 v[66:81], v[130:133], v[94:97], v[66:81]
	s_waitcnt lgkmcnt(6)
	v_mfma_f32_32x32x16_bf16 v[66:81], v[134:137], v[90:93], v[66:81]
	s_waitcnt lgkmcnt(5)
	v_mfma_f32_32x32x16_bf16 v[66:81], v[142:145], v[86:89], v[66:81]
	s_waitcnt lgkmcnt(4)
	v_mfma_f32_32x32x16_bf16 v[66:81], v[146:149], v[122:125], v[66:81]
	v_lshl_add_u64 v[138:139], s[26:27], 0, v[196:197]
	v_lshl_add_u64 v[130:131], s[26:27], 0, v[192:193]
	v_lshl_add_u64 v[132:133], s[26:27], 0, v[194:195]
	v_lshl_add_u64 v[134:135], s[26:27], 0, v[190:191]
	v_lshl_add_u64 v[136:137], s[26:27], 0, v[198:199]
	s_waitcnt lgkmcnt(3)
	v_mfma_f32_32x32x16_bf16 v[66:81], v[222:225], v[118:121], v[66:81]
	global_load_dwordx4 v[146:149], v[134:135], off
	global_load_dwordx4 v[142:145], v[136:137], off
	s_nop 0
	global_load_dwordx4 v[138:141], v[138:139], off
	s_nop 0
	global_load_dwordx4 v[134:137], v[130:131], off
	s_nop 0
	global_load_dwordx4 v[130:133], v[132:133], off
	s_waitcnt lgkmcnt(2)
	v_mfma_f32_32x32x16_bf16 v[66:81], v[226:229], v[114:117], v[66:81]
	s_waitcnt lgkmcnt(1)
	v_mfma_f32_32x32x16_bf16 v[66:81], v[248:251], v[110:113], v[66:81]
	s_waitcnt lgkmcnt(0)
	v_mfma_f32_32x32x16_bf16 v[66:81], v[252:255], v[82:85], v[66:81]
	s_nop 11
	v_max3_f32 v222, v66, s16, v67
	v_max3_f32 v222, v222, v68, v69
	v_max3_f32 v222, v222, v70, v71
	v_max3_f32 v222, v222, v72, v73
	v_max3_f32 v222, v222, v74, v75
	v_max3_f32 v222, v222, v76, v77
	v_max3_f32 v222, v222, v78, v79
	v_max3_f32 v222, v222, v80, v81
	v_mov_b32_e32 v223, v222
	s_nop 1
	v_permlane32_swap_b32_e32 v222, v223
	v_mul_f32_e32 v222, 0x3dd53b95, v222
	v_max_f32_e32 v187, v187, v222
	v_fma_f32 v66, v66, s17, -v187
	v_fma_f32 v67, v67, s17, -v187
	v_fma_f32 v229, v81, s17, -v187
	v_exp_f32_e32 v81, v66
	v_fma_f32 v68, v68, s17, -v187
	v_exp_f32_e32 v222, v67
	v_fma_f32 v69, v69, s17, -v187
	v_fma_f32 v227, v79, s17, -v187
	v_exp_f32_e32 v79, v68
	v_sub_f32_e32 v223, v189, v187
	v_fma_f32 v70, v70, s17, -v187
	v_fma_f32 v73, v73, s17, -v187
	v_fma_f32 v75, v75, s17, -v187
	v_exp_f32_e32 v189, v69
	v_fma_f32 v71, v71, s17, -v187
	v_fma_f32 v225, v77, s17, -v187
	v_fma_f32 v226, v78, s17, -v187
	v_exp_f32_e32 v77, v70
	v_exp_f32_e32 v78, v73
	v_exp_f32_e32 v73, v75
	v_add_f32_e32 v75, 0, v81
	v_fma_f32 v72, v72, s17, -v187
	v_fma_f32 v228, v80, s17, -v187
	v_exp_f32_e32 v80, v71
	v_add_f32_e32 v75, v222, v75
	v_fma_f32 v224, v76, s17, -v187
	v_exp_f32_e32 v76, v72
	v_add_f32_e32 v75, v79, v75
	v_fma_f32 v74, v74, s17, -v187
	v_add_f32_e32 v75, v189, v75
	v_exp_f32_e32 v70, v74
	v_add_f32_e32 v75, v77, v75
	v_add_f32_e32 v75, v80, v75
	v_exp_f32_e32 v68, v224
	v_add_f32_e32 v75, v76, v75
	v_exp_f32_e32 v71, v225
	v_add_f32_e32 v75, v78, v75
	v_exp_f32_e32 v67, v226
	v_add_f32_e32 v75, v70, v75
	v_exp_f32_e32 v69, v227
	v_add_f32_e32 v75, v73, v75
	v_exp_f32_e32 v72, v228
	v_add_f32_e32 v75, v68, v75
	v_exp_f32_e32 v74, v229
	v_add_f32_e32 v75, v71, v75
	v_add_f32_e32 v75, v67, v75
	v_exp_f32_e32 v66, v223
	v_add_f32_e32 v75, v69, v75
	v_add_f32_e32 v75, v72, v75
	v_add_f32_e32 v75, v74, v75
	v_mov_b32_e32 v223, v75
	v_cmp_neq_f32_e32 vcc, 1.0, v66
	s_nop 0
	v_permlane32_swap_b32_e32 v75, v223
	s_cbranch_vccz .LBB0_3208
	v_pk_mul_f32 v[64:65], v[64:65], v[66:67] op_sel_hi:[1,0]
	v_pk_mul_f32 v[62:63], v[62:63], v[66:67] op_sel_hi:[1,0]
	v_pk_mul_f32 v[60:61], v[60:61], v[66:67] op_sel_hi:[1,0]
	v_pk_mul_f32 v[58:59], v[58:59], v[66:67] op_sel_hi:[1,0]
	v_pk_mul_f32 v[56:57], v[56:57], v[66:67] op_sel_hi:[1,0]
	v_pk_mul_f32 v[54:55], v[54:55], v[66:67] op_sel_hi:[1,0]
	v_pk_mul_f32 v[52:53], v[52:53], v[66:67] op_sel_hi:[1,0]
	v_pk_mul_f32 v[50:51], v[50:51], v[66:67] op_sel_hi:[1,0]
	v_pk_mul_f32 v[48:49], v[48:49], v[66:67] op_sel_hi:[1,0]
	v_pk_mul_f32 v[46:47], v[46:47], v[66:67] op_sel_hi:[1,0]
	v_pk_mul_f32 v[44:45], v[44:45], v[66:67] op_sel_hi:[1,0]
	v_pk_mul_f32 v[42:43], v[42:43], v[66:67] op_sel_hi:[1,0]
	v_pk_mul_f32 v[40:41], v[40:41], v[66:67] op_sel_hi:[1,0]
	v_pk_mul_f32 v[38:39], v[38:39], v[66:67] op_sel_hi:[1,0]
	v_pk_mul_f32 v[36:37], v[36:37], v[66:67] op_sel_hi:[1,0]
	v_pk_mul_f32 v[34:35], v[34:35], v[66:67] op_sel_hi:[1,0]
	v_pk_mul_f32 v[32:33], v[32:33], v[66:67] op_sel_hi:[1,0]
	v_pk_mul_f32 v[30:31], v[30:31], v[66:67] op_sel_hi:[1,0]
	v_pk_mul_f32 v[28:29], v[28:29], v[66:67] op_sel_hi:[1,0]
	v_pk_mul_f32 v[26:27], v[26:27], v[66:67] op_sel_hi:[1,0]
	v_pk_mul_f32 v[24:25], v[24:25], v[66:67] op_sel_hi:[1,0]
	v_pk_mul_f32 v[22:23], v[22:23], v[66:67] op_sel_hi:[1,0]
	v_pk_mul_f32 v[20:21], v[20:21], v[66:67] op_sel_hi:[1,0]
	v_pk_mul_f32 v[18:19], v[18:19], v[66:67] op_sel_hi:[1,0]
	v_pk_mul_f32 v[16:17], v[16:17], v[66:67] op_sel_hi:[1,0]
	v_pk_mul_f32 v[14:15], v[14:15], v[66:67] op_sel_hi:[1,0]
	v_pk_mul_f32 v[12:13], v[12:13], v[66:67] op_sel_hi:[1,0]
	v_pk_mul_f32 v[10:11], v[10:11], v[66:67] op_sel_hi:[1,0]
	v_pk_mul_f32 v[8:9], v[8:9], v[66:67] op_sel_hi:[1,0]
	v_pk_mul_f32 v[6:7], v[6:7], v[66:67] op_sel_hi:[1,0]
	v_pk_mul_f32 v[4:5], v[4:5], v[66:67] op_sel_hi:[1,0]
	v_pk_mul_f32 v[2:3], v[2:3], v[66:67] op_sel_hi:[1,0]
.LBB0_3208:
	s_add_i32 s24, s19, s24
	v_cvt_pk_bf16_f32 v222, v81, v222
	v_cvt_pk_bf16_f32 v223, v79, v189
	v_cvt_pk_bf16_f32 v224, v77, v80
	v_cvt_pk_bf16_f32 v225, v76, v78
	v_add_f32_e32 v189, v75, v75
	v_fmac_f32_e32 v189, v221, v66
	v_cvt_pk_bf16_f32 v226, v70, v73
	v_cvt_pk_bf16_f32 v227, v68, v71
	v_cvt_pk_bf16_f32 v228, v67, v69
	v_cvt_pk_bf16_f32 v229, v72, v74
	v_add3_u32 v80, s24, v210, v200
	v_add_u32_e32 v81, 0x6000, v80
	v_add_u32_e32 v230, 0x7000, v80
	v_add_u32_e32 v231, 0x8800, v80
	v_add_u32_e32 v80, 0x9800, v80
	ds_read2_b64 v[66:69], v81 offset0:128 offset1:130
	ds_read2_b64 v[70:73], v230 offset0:192 offset1:194
	ds_read2_b64 v[74:77], v231 offset1:2
	ds_read2_b64 v[248:251], v80 offset0:64 offset1:66
	ds_read2_b64 v[252:255], v81 offset0:132 offset1:134
	s_add_i32 s23, s23, 1
	s_bitcmp1_b32 s23, 0
	s_cselect_b32 s24, 0xac00, 0
	s_add_i32 s24, s24, 0
	s_waitcnt lgkmcnt(4)
	v_mfma_f32_32x32x16_bf16 v[50:65], v[66:69], v[222:225], v[50:65]
	ds_read2_b64 v[66:69], v230 offset0:196 offset1:198
	v_lshl_add_u64 v[190:191], v[190:191], 0, s[8:9]
	s_waitcnt lgkmcnt(4)
	v_mfma_f32_32x32x16_bf16 v[34:49], v[70:73], v[222:225], v[34:49]
	ds_read2_b64 v[70:73], v231 offset0:4 offset1:6
	v_lshl_add_u64 v[192:193], v[192:193], 0, s[10:11]
	v_lshl_add_u64 v[194:195], v[194:195], 0, s[10:11]
	s_waitcnt lgkmcnt(4)
	v_mfma_f32_32x32x16_bf16 v[18:33], v[74:77], v[222:225], v[18:33]
	ds_read2_b64 v[74:77], v80 offset0:68 offset1:70
	v_lshl_add_u64 v[196:197], v[196:197], 0, s[8:9]
	v_lshl_add_u64 v[198:199], v[198:199], 0, s[8:9]
	s_cmp_eq_u32 s23, 35
	s_waitcnt lgkmcnt(4)
	v_mfma_f32_32x32x16_bf16 v[2:17], v[248:251], v[222:225], v[2:17]
	s_waitcnt lgkmcnt(3)
	v_mfma_f32_32x32x16_bf16 v[50:65], v[252:255], v[226:229], v[50:65]
	s_waitcnt lgkmcnt(2)
	v_mfma_f32_32x32x16_bf16 v[34:49], v[66:69], v[226:229], v[34:49]
	s_waitcnt lgkmcnt(1)
	v_mfma_f32_32x32x16_bf16 v[18:33], v[70:73], v[226:229], v[18:33]
	s_waitcnt lgkmcnt(0)
	v_mfma_f32_32x32x16_bf16 v[2:17], v[74:77], v[226:229], v[2:17]
	v_add3_u32 v66, s24, v201, v202
	s_waitcnt vmcnt(4)
	ds_write_b128 v66, v[146:149]
	v_add3_u32 v66, s24, v203, v204
	s_waitcnt vmcnt(3)
	ds_write_b128 v66, v[142:145]
	v_add3_u32 v66, s24, v205, v206
	s_waitcnt vmcnt(2)
	ds_write_b128 v66, v[138:141]
	v_add_u32_e32 v66, s24, v207
	s_waitcnt vmcnt(1)
	ds_write_b128 v66, v[134:137] offset:25600
	v_add_u32_e32 v66, s24, v208
	s_waitcnt vmcnt(0)
	ds_write_b128 v66, v[130:133] offset:25600
	s_waitcnt lgkmcnt(0)
	s_barrier
	s_cbranch_scc1 .LBB0_3210
	v_mov_b32_e32 v221, v189
	s_branch .LBB0_3206
